# speedup vs baseline: 1.0287x; 1.0066x over previous
_Z11k_gemm_a1b3IN3pg87EpiQKV3EEvNS0_4GemmET_:
	s_load_dwordx4 s[4:7], s[0:1], 0x0
	s_load_dword s14, s[0:1], 0x18
	s_lshl_b32 s28, s2, 2
	s_and_b32 s3, s28, 24
	s_bfe_u32 s8, s2, 0x30003
	s_or_b32 s3, s3, s8
	s_and_b32 s30, s28, 4
	s_ashr_i32 s8, s2, 6
	s_waitcnt lgkmcnt(0)
	s_ashr_i32 s15, s14, 31
	s_add_i32 s30, s30, s8
	s_lshr_b32 s8, s15, 27
	v_readfirstlane_b32 s24, v0
	s_add_i32 s8, s14, s8
	s_ashr_i32 s8, s8, 5
	s_lshr_b32 s10, s24, 7
	s_bfe_u32 s9, s24, 0x10006
	s_mul_i32 s10, s10, s8
	s_lshr_b32 s25, s24, 6
	s_add_i32 s10, s10, s9
	s_lshl_b32 s36, s10, 10
	s_add_i32 s10, s25, 8
	s_lshr_b32 s10, s10, 1
	s_mul_i32 s8, s10, s8
	s_add_i32 s8, s8, s9
	s_lshl_b32 s17, s8, 10
	s_lshl_b64 s[12:13], s[14:15], 8
	s_lshr_b64 s[8:9], s[14:15], 24
	s_mul_i32 s8, s8, s3
	s_mul_hi_u32 s9, s12, s3
	s_lshr_b32 s33, s24, 8
	s_lshl_b32 s16, s25, 10
	s_add_i32 s9, s9, s8
	s_mul_i32 s8, s12, s3
	s_add_u32 s4, s4, s8
	s_mul_i32 s37, s30, 0x300
	s_addc_u32 s5, s5, s9
	s_mul_hi_i32 s35, s30, 0x300
	s_mul_hi_u32 s8, s37, s14
	s_mul_i32 s9, s37, s15
	v_lshlrev_b32_e32 v132, 4, v0
	s_add_i32 s8, s8, s9
	s_mul_i32 s9, s35, s14
	s_add_i32 s18, s16, 0
	v_and_b32_e32 v97, 0x3f0, v132
	s_add_i32 s9, s8, s9
	s_mul_i32 s8, s37, s14
	s_add_i32 s19, s18, 0x2000
	v_or_b32_e32 v130, s36, v97
	s_mov_b32 m0, s18
	s_add_u32 s8, s6, s8
	v_or_b32_e32 v98, s17, v97
	global_load_lds_dwordx4 v130, s[4:5]
	s_mov_b32 m0, s19
	s_addc_u32 s9, s7, s9
	s_add_i32 s20, s18, 0x4000
	s_add_i32 s21, s18, 0x6000
	global_load_lds_dwordx4 v98, s[4:5]
	s_mov_b32 m0, s20
	s_add_u32 s10, s8, s12
	global_load_lds_dwordx4 v130, s[8:9]
	s_mov_b32 m0, s21
	s_addc_u32 s11, s9, s13
	s_add_i32 s22, s18, 0x8000
	s_add_i32 s23, s18, 0xa000
	global_load_lds_dwordx4 v98, s[8:9]
	s_mov_b32 m0, s22
	s_add_u32 s12, s10, s12
	global_load_lds_dwordx4 v130, s[10:11]
	s_mov_b32 m0, s23
	s_addc_u32 s13, s11, s13
	s_add_i32 s26, s18, 0xc000
	v_mov_b32_e32 v131, 0
	global_load_lds_dwordx4 v98, s[10:11]
	s_mov_b32 m0, s26
	s_add_i32 s27, s18, 0xe000
	v_lshl_add_u64 v[2:3], s[4:5], 0, v[130:131]
	v_mov_b32_e32 v99, v131
	global_load_lds_dwordx4 v130, s[12:13]
	s_mov_b32 m0, s27
	s_mov_b64 s[38:39], 0x800
	v_lshl_add_u64 v[4:5], s[4:5], 0, v[98:99]
	global_load_lds_dwordx4 v98, s[12:13]
	s_add_i32 m0, s18, 0x10000
	v_lshl_add_u64 v[2:3], v[2:3], 0, s[38:39]
	v_lshl_add_u64 v[6:7], s[8:9], 0, v[130:131]
	global_load_lds_dwordx4 v[2:3], off
	v_lshl_add_u64 v[2:3], v[4:5], 0, s[38:39]
	s_add_i32 m0, s18, 0x12000
	v_lshl_add_u64 v[8:9], s[8:9], 0, v[98:99]
	global_load_lds_dwordx4 v[2:3], off
	s_add_i32 m0, s18, 0x14000
	v_lshl_add_u64 v[2:3], v[6:7], 0, s[38:39]
	global_load_lds_dwordx4 v[2:3], off
	v_lshl_add_u64 v[2:3], v[8:9], 0, s[38:39]
	s_add_i32 m0, s18, 0x16000
	s_cmp_lg_u32 s33, 1
	global_load_lds_dwordx4 v[2:3], off
	v_mov_b32_e32 v96, 0
	v_mov_b32_e32 v95, 0
	v_mov_b32_e32 v94, 0
	v_mov_b32_e32 v93, 0
	v_mov_b32_e32 v92, 0
	v_mov_b32_e32 v91, 0
	v_mov_b32_e32 v90, 0
	v_mov_b32_e32 v89, 0
	v_mov_b32_e32 v88, 0
	v_mov_b32_e32 v87, 0
	v_mov_b32_e32 v86, 0
	v_mov_b32_e32 v85, 0
	v_mov_b32_e32 v84, 0
	v_mov_b32_e32 v83, 0
	v_mov_b32_e32 v82, 0
	v_mov_b32_e32 v81, 0
	v_mov_b32_e32 v80, 0
	v_mov_b32_e32 v79, 0
	v_mov_b32_e32 v78, 0
	v_mov_b32_e32 v77, 0
	v_mov_b32_e32 v76, 0
	v_mov_b32_e32 v75, 0
	v_mov_b32_e32 v74, 0
	v_mov_b32_e32 v73, 0
	v_mov_b32_e32 v72, 0
	v_mov_b32_e32 v71, 0
	v_mov_b32_e32 v70, 0
	v_mov_b32_e32 v69, 0
	v_mov_b32_e32 v68, 0
	v_mov_b32_e32 v67, 0
	v_mov_b32_e32 v66, 0
	v_mov_b32_e32 v65, 0
	v_mov_b32_e32 v64, 0
	v_mov_b32_e32 v63, 0
	v_mov_b32_e32 v62, 0
	v_mov_b32_e32 v61, 0
	v_mov_b32_e32 v60, 0
	v_mov_b32_e32 v59, 0
	v_mov_b32_e32 v58, 0
	v_mov_b32_e32 v57, 0
	v_mov_b32_e32 v56, 0
	v_mov_b32_e32 v55, 0
	v_mov_b32_e32 v54, 0
	v_mov_b32_e32 v53, 0
	v_mov_b32_e32 v52, 0
	v_mov_b32_e32 v51, 0
	v_mov_b32_e32 v50, 0
	v_mov_b32_e32 v49, 0
	v_mov_b32_e32 v48, 0
	v_mov_b32_e32 v47, 0
	v_mov_b32_e32 v46, 0
	v_mov_b32_e32 v45, 0
	v_mov_b32_e32 v44, 0
	v_mov_b32_e32 v43, 0
	v_mov_b32_e32 v42, 0
	v_mov_b32_e32 v41, 0
	v_mov_b32_e32 v40, 0
	v_mov_b32_e32 v39, 0
	v_mov_b32_e32 v38, 0
	v_mov_b32_e32 v37, 0
	v_mov_b32_e32 v36, 0
	v_mov_b32_e32 v35, 0
	v_mov_b32_e32 v34, 0
	v_mov_b32_e32 v33, 0
	v_mov_b32_e32 v32, 0
	v_mov_b32_e32 v31, 0
	v_mov_b32_e32 v30, 0
	v_mov_b32_e32 v29, 0
	v_mov_b32_e32 v28, 0
	v_mov_b32_e32 v27, 0
	v_mov_b32_e32 v26, 0
	v_mov_b32_e32 v25, 0
	v_mov_b32_e32 v24, 0
	v_mov_b32_e32 v23, 0
	v_mov_b32_e32 v22, 0
	v_mov_b32_e32 v21, 0
	v_mov_b32_e32 v20, 0
	v_mov_b32_e32 v19, 0
	v_mov_b32_e32 v18, 0
	v_mov_b32_e32 v17, 0
	v_mov_b32_e32 v16, 0
	v_mov_b32_e32 v15, 0
	v_mov_b32_e32 v14, 0
	v_mov_b32_e32 v13, 0
	v_mov_b32_e32 v12, 0
	v_mov_b32_e32 v11, 0
	v_mov_b32_e32 v10, 0
	v_mov_b32_e32 v9, 0
	v_mov_b32_e32 v8, 0
	v_mov_b32_e32 v7, 0
	v_mov_b32_e32 v6, 0
	v_mov_b32_e32 v5, 0
	v_mov_b32_e32 v4, 0
	v_mov_b32_e32 v3, 0
	v_mov_b32_e32 v2, 0
	s_cbranch_scc1 .LBB2_2
	s_barrier
.LBB2_2:
	s_waitcnt vmcnt(8)
	s_and_b32 s31, s25, 3
	s_lshl_b32 s25, s33, 6
	v_and_b32_e32 v1, 15, v0
	s_mov_b32 s29, 3
	s_cmp_lt_i32 s14, 64
	v_or_b32_e32 v133, s25, v1
	s_barrier
	s_barrier
	s_cbranch_scc1 .LBB2_6
	v_and_b32_e32 v2, 48, v0
	v_lshlrev_b32_e32 v3, 6, v133
	s_movk_i32 s34, 0x3c0
	v_lshlrev_b32_e32 v4, 2, v133
	v_and_or_b32 v3, v3, s34, v2
	v_and_b32_e32 v4, 32, v4
	s_lshl_b32 s33, s33, 13
	v_lshlrev_b32_e32 v5, 6, v0
	v_bitop3_b32 v8, v3, s33, v4 bitop3:0xde
	s_lshr_b32 s33, s15, 26
	v_and_or_b32 v2, v5, s34, v2
	v_lshlrev_b32_e32 v5, 2, v0
	s_add_i32 s33, s14, s33
	v_and_b32_e32 v5, 32, v5
	s_lshl_b32 s34, s31, 12
	s_ashr_i32 s33, s33, 6
	v_bitop3_b32 v9, s34, v2, v5 bitop3:0xf6
	s_add_i32 s34, s33, -1
	s_add_u32 s40, s37, 0x100
	s_addc_u32 s41, s35, 0
	v_add_u32_e32 v2, s36, v97
	v_mov_b32_e32 v3, 0
	v_mov_b32_e32 v10, s14
	s_mul_i32 s41, s41, s14
	s_mul_i32 s36, s40, s15
	v_mad_u64_u32 v[4:5], s[38:39], s40, v10, v[2:3]
	s_add_i32 s36, s36, s41
	v_add_u32_e32 v5, s36, v5
	s_mov_b64 s[38:39], 0x800
	v_lshl_add_u64 v[100:101], v[4:5], 0, s[38:39]
	v_add_u32_e32 v4, s17, v97
	v_mov_b32_e32 v5, v3
	s_add_u32 s17, s37, 0x200
	v_mad_u64_u32 v[6:7], s[40:41], s40, v10, v[4:5]
	s_addc_u32 s35, s35, 0
	v_add_u32_e32 v7, s36, v7
	s_mul_i32 s35, s35, s14
	s_mul_i32 s14, s17, s15
	v_lshl_add_u64 v[102:103], v[6:7], 0, s[38:39]
	v_mad_u64_u32 v[6:7], s[36:37], s17, v10, v[2:3]
	s_add_i32 s35, s14, s35
	v_mad_u64_u32 v[4:5], s[14:15], s17, v10, v[4:5]
	v_add_u32_e32 v7, s35, v7
	v_add_u32_e32 v5, s35, v5
	v_lshl_add_u64 v[104:105], v[6:7], 0, s[38:39]
	v_lshl_add_u64 v[106:107], v[4:5], 0, s[38:39]
	s_add_i32 s14, 0, 0x18000
	s_add_i32 s15, 0, 0x1c000
	s_add_i32 s41, 0, 0x14000
	s_add_i32 s39, 0, 0x10000
	s_add_i32 s35, s14, s16
	s_add_i32 s37, s15, s16
	v_add_u32_e32 v110, s41, v9
	v_add_u32_e32 v111, s39, v8
	s_add_i32 s39, s39, s16
	s_add_i32 s41, s41, s16
	v_add_u32_e32 v108, 0, v9
	v_add_u32_e32 v109, 0, v8
	s_add_i32 s36, s35, 0x2000
	s_add_i32 s38, s37, 0x2000
	v_add_u32_e32 v112, s14, v9
	v_add_u32_e32 v113, s15, v9
	s_add_i32 s40, s39, 0x2000
	s_add_i32 s42, s41, 0x2000
	v_mov_b32_e32 v2, v3
	v_mov_b32_e32 v4, v3
	v_mov_b32_e32 v5, v3
	v_mov_b32_e32 v6, v3
	v_mov_b32_e32 v7, v3
	v_mov_b32_e32 v8, v3
	v_mov_b32_e32 v9, v3
	v_mov_b32_e32 v10, v3
	v_mov_b32_e32 v97, v3

.LBB3_2:
	s_mov_b64 s[16:17], 0x800
	v_lshl_add_u64 v[12:13], v[12:13], 0, s[16:17]
	s_add_i32 m0, s14, 0xc000
	s_waitcnt vmcnt(2)
	s_barrier
	global_load_lds_dwordx4 v[12:13], off
	v_lshl_add_u64 v[10:11], v[10:11], 0, s[16:17]
	s_add_i32 m0, s14, 0xe000
	v_lshl_add_u64 v[8:9], v[8:9], 0, s[16:17]
	global_load_lds_dwordx4 v[10:11], off
	s_add_i32 m0, s14, 0x10000
	v_lshl_add_u64 v[6:7], v[6:7], 0, s[16:17]
	global_load_lds_dwordx4 v[8:9], off
	s_add_i32 m0, s14, 0x12000
	v_lshl_add_u64 v[4:5], v[4:5], 0, s[16:17]
	global_load_lds_dwordx4 v[6:7], off
	s_add_i32 m0, s14, 0x14000
	v_lshl_add_u64 v[2:3], v[2:3], 0, s[16:17]
	global_load_lds_dwordx4 v[4:5], off
	s_add_i32 m0, s14, 0x16000
	s_lshl_b32 s13, s13, 5
	global_load_lds_dwordx4 v[2:3], off
	v_and_b32_e32 v1, 15, v0
	s_and_b32 s13, s13, 0x60
	v_lshl_or_b32 v1, s15, 6, v1
	s_cmp_lt_i32 s8, 64
	v_mov_b32_e32 v4, 0
	v_mov_b32_e32 v3, 0
	v_mov_b32_e32 v2, 0
	v_mov_b32_e32 v21, 0
	v_mov_b32_e32 v20, 0
	v_mov_b32_e32 v19, 0
	v_mov_b32_e32 v18, 0
	v_mov_b32_e32 v9, 0
	v_mov_b32_e32 v8, 0
	v_mov_b32_e32 v7, 0
	v_mov_b32_e32 v6, 0
	v_mov_b32_e32 v25, 0
	v_mov_b32_e32 v24, 0
	v_mov_b32_e32 v23, 0
	v_mov_b32_e32 v22, 0
	v_mov_b32_e32 v13, 0
	v_mov_b32_e32 v12, 0
	v_mov_b32_e32 v11, 0
	v_mov_b32_e32 v10, 0
	v_mov_b32_e32 v33, 0
	v_mov_b32_e32 v32, 0
	v_mov_b32_e32 v31, 0
	v_mov_b32_e32 v30, 0
	v_mov_b32_e32 v17, 0
	v_mov_b32_e32 v16, 0
	v_mov_b32_e32 v15, 0
	v_mov_b32_e32 v14, 0
	v_mov_b32_e32 v37, 0
	v_mov_b32_e32 v36, 0
	v_mov_b32_e32 v35, 0
	v_mov_b32_e32 v34, 0
	v_mov_b32_e32 v65, 0
	v_mov_b32_e32 v64, 0
	v_mov_b32_e32 v63, 0
	v_mov_b32_e32 v62, 0
	v_mov_b32_e32 v49, 0
	v_mov_b32_e32 v48, 0
	v_mov_b32_e32 v47, 0
	v_mov_b32_e32 v46, 0
	v_mov_b32_e32 v61, 0
	v_mov_b32_e32 v60, 0
	v_mov_b32_e32 v59, 0
	v_mov_b32_e32 v58, 0
	v_mov_b32_e32 v45, 0
	v_mov_b32_e32 v44, 0
	v_mov_b32_e32 v43, 0
	v_mov_b32_e32 v42, 0
	v_mov_b32_e32 v57, 0
	v_mov_b32_e32 v56, 0
	v_mov_b32_e32 v55, 0
	v_mov_b32_e32 v54, 0
	v_mov_b32_e32 v41, 0
	v_mov_b32_e32 v40, 0
	v_mov_b32_e32 v39, 0
	v_mov_b32_e32 v38, 0
	v_mov_b32_e32 v53, 0
	v_mov_b32_e32 v52, 0
	v_mov_b32_e32 v51, 0
	v_mov_b32_e32 v50, 0
	v_mov_b32_e32 v29, 0
	v_mov_b32_e32 v28, 0
	v_mov_b32_e32 v27, 0
	v_mov_b32_e32 v26, 0
	s_barrier
	s_cbranch_scc1 .LBB3_6
	v_and_b32_e32 v2, 48, v0
	v_lshlrev_b32_e32 v3, 6, v1
	s_movk_i32 s16, 0x3c0
	v_lshlrev_b32_e32 v4, 2, v1
	s_lshl_b32 s17, s15, 13
	v_and_or_b32 v3, v3, s16, v2
	v_and_b32_e32 v4, 32, v4
	s_add_i32 s17, s17, 0
	v_xad_u32 v67, v3, v4, s17
	v_lshlrev_b32_e32 v3, 6, v0
	v_and_or_b32 v2, v3, s16, v2
	v_lshlrev_b32_e32 v3, 2, v0
	s_lshr_b32 s9, s9, 26
	v_and_b32_e32 v3, 32, v3
	s_lshl_b32 s16, s13, 7
	s_add_i32 s8, s8, s9
	s_ashr_i32 s8, s8, 6
	v_bitop3_b32 v2, s16, v2, v3 bitop3:0xf6
	v_mov_b32_e32 v26, 0
	s_mov_b32 s15, 0
	s_add_i32 s9, s8, -1
	v_add_u32_e32 v72, 0, v2
	s_mov_b32 s17, 0x18000
	s_mov_b32 s16, 0
	v_mov_b32_e32 v2, v26
	v_mov_b32_e32 v3, v26
	v_mov_b32_e32 v4, v26
	v_mov_b32_e32 v5, v26
